# baseline (speedup 1.0000x reference)
.LBB0_4:
	s_load_dwordx4 s[20:23], s[0:1], 0x38
	s_load_dwordx2 s[18:19], s[0:1], 0x48
	s_ashr_i32 s2, s2, 3
	s_add_i32 s2, s3, s2
	s_ashr_i32 s33, s2, 3
	s_waitcnt lgkmcnt(0)
	s_mul_i32 s33, s33, s21
	s_mul_i32 s69, s33, s20
	v_bfe_u32 v18, v0, 2, 6
	v_lshrrev_b32_e32 v40, 8, v0
	v_sub_u32_e32 v41, 1, v40
	v_mul_u32_u24_e32 v18, v18, v41
	s_and_b32 s3, s2, 7
	v_add_u32_e32 v2, s69, v18
	s_add_i32 s2, s22, -1
	v_min_i32_e32 v2, s2, v2
	v_ashrrev_i32_e32 v3, 31, v2
	v_lshlrev_b64 v[6:7], 10, v[2:3]
	v_lshlrev_b32_e32 v2, 4, v0
	v_and_b32_e32 v19, 48, v2
	v_mul_u32_u24_e32 v19, v19, v41
	v_or_b32_e32 v6, v6, v19
	v_lshl_add_u64 v[36:37], s[8:9], 0, v[6:7]
	global_load_dwordx4 v[2:5], v[36:37], off
	v_lshl_add_u64 v[34:35], s[10:11], 0, v[6:7]
	global_load_dwordx4 v[6:9], v[34:35], off
	v_lshrrev_b32_e32 v40, 7, v0
	v_and_b32_e32 v1, 63, v0
	v_bfe_u32 v41, v0, 6, 1
	v_lshlrev_b32_e32 v10, 4, v40
	s_lshl_b32 s2, s3, 1
	v_or3_b32 v10, s2, v10, v41
	v_lshlrev_b32_e32 v11, 3, v1
	s_lshl_b32 s22, s3, 6
	v_and_b32_e32 v42, 31, v0
	v_lshl_or_b32 v14, v10, 14, v11
	v_lshl_or_b32 v10, v40, 9, s22
	v_lshlrev_b32_e32 v11, 5, v41
	v_or3_b32 v10, v10, v11, v42
	v_lshlrev_b32_e32 v15, 2, v10
	global_load_dword v39, v15, s[12:13]
	global_load_dwordx4 v[10:13], v[36:37], off offset:64
	v_lshlrev_b32_e32 v46, 1, v14
	global_load_dwordx4 v[48:51], v46, s[4:5]
	global_load_dwordx4 v[14:17], v[34:35], off offset:64
	global_load_dwordx4 v[52:55], v46, s[6:7]
	global_load_dwordx4 v[56:59], v46, s[4:5] offset:1024
	global_load_dwordx4 v[60:63], v46, s[6:7] offset:1024
	global_load_dwordx4 v[64:67], v46, s[4:5] offset:2048
	global_load_dwordx4 v[68:71], v46, s[6:7] offset:2048
	global_load_dwordx4 v[72:75], v[36:37], off offset:128
	global_load_dwordx4 v[76:79], v[34:35], off offset:128
	v_bfe_u32 v43, v0, 5, 1
	v_mul_u32_u24_e32 v18, 40, v18
	v_mul_u32_u24_e32 v20, 0x50, v42
	v_lshl_add_u32 v44, v18, 1, v19
	v_lshl_add_u32 v45, v43, 4, v20
	v_lshrrev_b32_e32 v20, 8, v0
	v_mul_u32_u24_e32 v20, 0xa000, v20
	v_add_u32_e32 v44, v44, v20
	v_lshrrev_b32_e32 v38, 6, v0
	s_waitcnt vmcnt(12)
	ds_write_b128 v44, v[2:5]
	s_waitcnt vmcnt(11)
	ds_write_b128 v44, v[6:9] offset:5120
	s_waitcnt lgkmcnt(0)
	s_barrier
	ds_read_b128 v[2:5], v45 offset:5120
	ds_read_b128 v[6:9], v45 offset:7680
	ds_read_b128 v[80:83], v45
	ds_read_b128 v[84:87], v45 offset:2560
	ds_read_b128 v[88:91], v45 offset:5152
	s_waitcnt vmcnt(8) lgkmcnt(4)
	v_mfma_f32_32x32x16_f16 v[18:33], v[2:5], v[48:51], 0
	ds_read_b128 v[92:95], v45 offset:32
	ds_write_b128 v44, v[10:13] offset:10240
	s_waitcnt vmcnt(6) lgkmcnt(4)
	v_mfma_f32_32x32x16_f16 v[18:33], v[80:83], v[52:55], v[18:33]
	ds_read_b128 v[96:99], v45 offset:7712
	v_mfma_f32_32x32x16_f16 v[18:33], v[80:83], v[48:51], v[18:33]
	ds_read_b128 v[80:83], v45 offset:2592
	ds_write_b128 v44, v[14:17] offset:15360
	v_mfma_f32_32x32x16_f16 v[2:17], v[6:9], v[48:51], 0
	global_load_dwordx4 v[100:103], v46, s[4:5] offset:3072
	global_load_dwordx4 v[104:107], v46, s[6:7] offset:3072
	s_waitcnt lgkmcnt(6)
	v_mfma_f32_32x32x16_f16 v[2:17], v[84:87], v[52:55], v[2:17]
	v_mfma_f32_32x32x16_f16 v[2:17], v[84:87], v[48:51], v[2:17]
	s_waitcnt lgkmcnt(0)
	s_barrier
	ds_read_b128 v[48:51], v45 offset:15360
	v_or_b32_e32 v47, 0x1000, v46
	s_waitcnt vmcnt(7)
	v_mfma_f32_32x32x16_f16 v[18:33], v[88:91], v[56:59], v[18:33]
	global_load_dwordx4 v[52:55], v[36:37], off offset:192
	ds_read_b128 v[84:87], v45 offset:10240
	s_waitcnt vmcnt(7)
	v_mfma_f32_32x32x16_f16 v[18:33], v[92:95], v[60:63], v[18:33]
	ds_read_b128 v[88:91], v45 offset:17920
	v_mfma_f32_32x32x16_f16 v[18:33], v[92:95], v[56:59], v[18:33]
	global_load_dwordx4 v[92:95], v[34:35], off offset:192
	ds_read_b128 v[108:111], v45 offset:12800
	v_mfma_f32_32x32x16_f16 v[2:17], v[96:99], v[56:59], v[2:17]
	global_load_dwordx4 v[96:99], v47, s[4:5]
	global_load_dwordx4 v[112:115], v47, s[6:7]
	v_mfma_f32_32x32x16_f16 v[2:17], v[80:83], v[60:63], v[2:17]
	v_mfma_f32_32x32x16_f16 v[2:17], v[80:83], v[56:59], v[2:17]
	ds_read_b128 v[56:59], v45 offset:15392
	v_or_b32_e32 v47, 0x1400, v46
	s_waitcnt vmcnt(9) lgkmcnt(4)
	v_mfma_f32_32x32x16_f16 v[18:33], v[48:51], v[64:67], v[18:33]
	ds_read_b128 v[48:51], v45 offset:10272
	s_waitcnt vmcnt(7)
	ds_write_b128 v44, v[72:75]
	s_waitcnt lgkmcnt(5)
	v_mfma_f32_32x32x16_f16 v[18:33], v[84:87], v[68:71], v[18:33]
	ds_read_b128 v[60:63], v45 offset:17952
	v_mfma_f32_32x32x16_f16 v[18:33], v[84:87], v[64:67], v[18:33]
	ds_read_b128 v[72:75], v45 offset:12832
	s_waitcnt vmcnt(6)
	ds_write_b128 v44, v[76:79] offset:5120
	s_waitcnt lgkmcnt(7)
	v_mfma_f32_32x32x16_f16 v[2:17], v[88:91], v[64:67], v[2:17]
	global_load_dwordx4 v[76:79], v47, s[4:5]
	global_load_dwordx4 v[80:83], v47, s[6:7]
	s_waitcnt lgkmcnt(6)
	v_mfma_f32_32x32x16_f16 v[2:17], v[108:111], v[68:71], v[2:17]
	v_mfma_f32_32x32x16_f16 v[2:17], v[108:111], v[64:67], v[2:17]
	s_waitcnt lgkmcnt(0)
	s_barrier
	ds_read_b128 v[64:67], v45 offset:5120
	v_or_b32_e32 v47, 0x1800, v46
	s_waitcnt vmcnt(7)
	v_mfma_f32_32x32x16_f16 v[18:33], v[56:59], v[100:103], v[18:33]
	global_load_dwordx4 v[56:59], v[36:37], off offset:256
	ds_read_b128 v[68:71], v45
	s_waitcnt vmcnt(7)
	v_mfma_f32_32x32x16_f16 v[18:33], v[48:51], v[104:107], v[18:33]
	ds_read_b128 v[84:87], v45 offset:7680
	v_mfma_f32_32x32x16_f16 v[18:33], v[48:51], v[100:103], v[18:33]
	global_load_dwordx4 v[48:51], v[34:35], off offset:256
	ds_read_b128 v[88:91], v45 offset:2560
	v_mfma_f32_32x32x16_f16 v[2:17], v[60:63], v[100:103], v[2:17]
	global_load_dwordx4 v[60:63], v47, s[4:5]
	global_load_dwordx4 v[108:111], v47, s[6:7]
	v_mfma_f32_32x32x16_f16 v[2:17], v[72:75], v[104:107], v[2:17]
	v_mfma_f32_32x32x16_f16 v[2:17], v[72:75], v[100:103], v[2:17]
	ds_read_b128 v[72:75], v45 offset:5152
	v_or_b32_e32 v47, 0x1c00, v46
	s_waitcnt vmcnt(7) lgkmcnt(4)
	v_mfma_f32_32x32x16_f16 v[18:33], v[64:67], v[96:99], v[18:33]
	ds_read_b128 v[64:67], v45 offset:32
	ds_write_b128 v44, v[52:55] offset:10240
	s_waitcnt vmcnt(6) lgkmcnt(5)
	v_mfma_f32_32x32x16_f16 v[18:33], v[68:71], v[112:115], v[18:33]
	ds_read_b128 v[52:55], v45 offset:7712
	v_mfma_f32_32x32x16_f16 v[18:33], v[68:71], v[96:99], v[18:33]
	ds_read_b128 v[68:71], v45 offset:2592
	ds_write_b128 v44, v[92:95] offset:15360
	s_waitcnt lgkmcnt(7)
	v_mfma_f32_32x32x16_f16 v[2:17], v[84:87], v[96:99], v[2:17]
	global_load_dwordx4 v[84:87], v47, s[4:5]
	global_load_dwordx4 v[92:95], v47, s[6:7]
	s_waitcnt lgkmcnt(6)
	v_mfma_f32_32x32x16_f16 v[2:17], v[88:91], v[112:115], v[2:17]
	v_mfma_f32_32x32x16_f16 v[2:17], v[88:91], v[96:99], v[2:17]
	s_waitcnt lgkmcnt(0)
	s_barrier
	ds_read_b128 v[88:91], v45 offset:15360
	v_or_b32_e32 v47, 0x2000, v46
	s_waitcnt vmcnt(7)
	v_mfma_f32_32x32x16_f16 v[18:33], v[72:75], v[76:79], v[18:33]
	global_load_dwordx4 v[72:75], v[36:37], off offset:320
	ds_read_b128 v[96:99], v45 offset:10240
	s_waitcnt vmcnt(7)
	v_mfma_f32_32x32x16_f16 v[18:33], v[64:67], v[80:83], v[18:33]
	ds_read_b128 v[100:103], v45 offset:17920
	v_mfma_f32_32x32x16_f16 v[18:33], v[64:67], v[76:79], v[18:33]
	global_load_dwordx4 v[64:67], v[34:35], off offset:320
	ds_read_b128 v[104:107], v45 offset:12800
	v_mfma_f32_32x32x16_f16 v[2:17], v[52:55], v[76:79], v[2:17]
	global_load_dwordx4 v[52:55], v47, s[4:5]
	global_load_dwordx4 v[112:115], v47, s[6:7]
	v_mfma_f32_32x32x16_f16 v[2:17], v[68:71], v[80:83], v[2:17]
	v_mfma_f32_32x32x16_f16 v[2:17], v[68:71], v[76:79], v[2:17]
	ds_read_b128 v[68:71], v45 offset:15392
	v_or_b32_e32 v47, 0x2400, v46
	s_waitcnt vmcnt(7) lgkmcnt(4)
	v_mfma_f32_32x32x16_f16 v[18:33], v[88:91], v[60:63], v[18:33]
	ds_read_b128 v[76:79], v45 offset:10272
	ds_write_b128 v44, v[56:59]
	s_waitcnt vmcnt(6) lgkmcnt(5)
	v_mfma_f32_32x32x16_f16 v[18:33], v[96:99], v[108:111], v[18:33]
	ds_read_b128 v[56:59], v45 offset:17952
	v_mfma_f32_32x32x16_f16 v[18:33], v[96:99], v[60:63], v[18:33]
	ds_read_b128 v[80:83], v45 offset:12832
	ds_write_b128 v44, v[48:51] offset:5120
	s_waitcnt lgkmcnt(7)
	v_mfma_f32_32x32x16_f16 v[2:17], v[100:103], v[60:63], v[2:17]
	global_load_dwordx4 v[48:51], v47, s[4:5]
	global_load_dwordx4 v[88:91], v47, s[6:7]
	s_waitcnt lgkmcnt(6)
	v_mfma_f32_32x32x16_f16 v[2:17], v[104:107], v[108:111], v[2:17]
	v_mfma_f32_32x32x16_f16 v[2:17], v[104:107], v[60:63], v[2:17]
	s_waitcnt lgkmcnt(0)
	s_barrier
	ds_read_b128 v[60:63], v45 offset:5120
	v_or_b32_e32 v47, 0x2800, v46
	s_waitcnt vmcnt(7)
	v_mfma_f32_32x32x16_f16 v[18:33], v[68:71], v[84:87], v[18:33]
	global_load_dwordx4 v[68:71], v[36:37], off offset:384
	ds_read_b128 v[96:99], v45
	s_waitcnt vmcnt(7)
	v_mfma_f32_32x32x16_f16 v[18:33], v[76:79], v[92:95], v[18:33]
	ds_read_b128 v[100:103], v45 offset:7680
	v_mfma_f32_32x32x16_f16 v[18:33], v[76:79], v[84:87], v[18:33]
	global_load_dwordx4 v[76:79], v[34:35], off offset:384
	ds_read_b128 v[104:107], v45 offset:2560
	v_mfma_f32_32x32x16_f16 v[2:17], v[56:59], v[84:87], v[2:17]
	global_load_dwordx4 v[56:59], v47, s[4:5]
	global_load_dwordx4 v[108:111], v47, s[6:7]
	v_mfma_f32_32x32x16_f16 v[2:17], v[80:83], v[92:95], v[2:17]
	v_mfma_f32_32x32x16_f16 v[2:17], v[80:83], v[84:87], v[2:17]
	ds_read_b128 v[80:83], v45 offset:5152
	v_or_b32_e32 v47, 0x2c00, v46
	s_waitcnt vmcnt(7) lgkmcnt(4)
	v_mfma_f32_32x32x16_f16 v[18:33], v[60:63], v[52:55], v[18:33]
	ds_read_b128 v[60:63], v45 offset:32
	ds_write_b128 v44, v[72:75] offset:10240
	s_waitcnt vmcnt(6) lgkmcnt(5)
	v_mfma_f32_32x32x16_f16 v[18:33], v[96:99], v[112:115], v[18:33]
	ds_read_b128 v[72:75], v45 offset:7712
	v_mfma_f32_32x32x16_f16 v[18:33], v[96:99], v[52:55], v[18:33]
	ds_read_b128 v[84:87], v45 offset:2592
	ds_write_b128 v44, v[64:67] offset:15360
	s_waitcnt lgkmcnt(7)
	v_mfma_f32_32x32x16_f16 v[2:17], v[100:103], v[52:55], v[2:17]
	global_load_dwordx4 v[64:67], v47, s[4:5]
	global_load_dwordx4 v[92:95], v47, s[6:7]
	s_waitcnt lgkmcnt(6)
	v_mfma_f32_32x32x16_f16 v[2:17], v[104:107], v[112:115], v[2:17]
	v_mfma_f32_32x32x16_f16 v[2:17], v[104:107], v[52:55], v[2:17]
	s_waitcnt lgkmcnt(0)
	s_barrier
	ds_read_b128 v[52:55], v45 offset:15360
	v_or_b32_e32 v47, 0x3000, v46
	s_waitcnt vmcnt(7)
	v_mfma_f32_32x32x16_f16 v[18:33], v[80:83], v[48:51], v[18:33]
	global_load_dwordx4 v[80:83], v[36:37], off offset:448
	ds_read_b128 v[96:99], v45 offset:10240
	s_waitcnt vmcnt(7)
	v_mfma_f32_32x32x16_f16 v[18:33], v[60:63], v[88:91], v[18:33]
	ds_read_b128 v[100:103], v45 offset:17920
	v_mfma_f32_32x32x16_f16 v[18:33], v[60:63], v[48:51], v[18:33]
	global_load_dwordx4 v[60:63], v[34:35], off offset:448
	ds_read_b128 v[104:107], v45 offset:12800
	v_mfma_f32_32x32x16_f16 v[2:17], v[72:75], v[48:51], v[2:17]
	global_load_dwordx4 v[72:75], v47, s[4:5]
	global_load_dwordx4 v[112:115], v47, s[6:7]
	v_mfma_f32_32x32x16_f16 v[2:17], v[84:87], v[88:91], v[2:17]
	v_mfma_f32_32x32x16_f16 v[2:17], v[84:87], v[48:51], v[2:17]
	ds_read_b128 v[48:51], v45 offset:15392
	v_or_b32_e32 v47, 0x3400, v46
	s_waitcnt vmcnt(7) lgkmcnt(4)
	v_mfma_f32_32x32x16_f16 v[18:33], v[52:55], v[56:59], v[18:33]
	ds_read_b128 v[52:55], v45 offset:10272
	ds_write_b128 v44, v[68:71]
	s_waitcnt vmcnt(6) lgkmcnt(5)
	v_mfma_f32_32x32x16_f16 v[18:33], v[96:99], v[108:111], v[18:33]
	ds_read_b128 v[68:71], v45 offset:17952
	v_mfma_f32_32x32x16_f16 v[18:33], v[96:99], v[56:59], v[18:33]
	ds_read_b128 v[84:87], v45 offset:12832
	ds_write_b128 v44, v[76:79] offset:5120
	s_waitcnt lgkmcnt(7)
	v_mfma_f32_32x32x16_f16 v[2:17], v[100:103], v[56:59], v[2:17]
	global_load_dwordx4 v[76:79], v47, s[4:5]
	global_load_dwordx4 v[88:91], v47, s[6:7]
	s_waitcnt lgkmcnt(6)
	v_mfma_f32_32x32x16_f16 v[2:17], v[104:107], v[108:111], v[2:17]
	v_mfma_f32_32x32x16_f16 v[2:17], v[104:107], v[56:59], v[2:17]
	s_waitcnt lgkmcnt(0)
	s_barrier
	ds_read_b128 v[56:59], v45 offset:5120
	v_or_b32_e32 v47, 0x3800, v46
	s_waitcnt vmcnt(7)
	v_mfma_f32_32x32x16_f16 v[18:33], v[48:51], v[64:67], v[18:33]
	global_load_dwordx4 v[48:51], v[36:37], off offset:512
	ds_read_b128 v[96:99], v45
	s_waitcnt vmcnt(7)
	v_mfma_f32_32x32x16_f16 v[18:33], v[52:55], v[92:95], v[18:33]
	ds_read_b128 v[100:103], v45 offset:7680
	v_mfma_f32_32x32x16_f16 v[18:33], v[52:55], v[64:67], v[18:33]
	global_load_dwordx4 v[52:55], v[34:35], off offset:512
	ds_read_b128 v[104:107], v45 offset:2560
	v_mfma_f32_32x32x16_f16 v[2:17], v[68:71], v[64:67], v[2:17]
	global_load_dwordx4 v[68:71], v47, s[4:5]
	global_load_dwordx4 v[108:111], v47, s[6:7]
	v_mfma_f32_32x32x16_f16 v[2:17], v[84:87], v[92:95], v[2:17]
	v_mfma_f32_32x32x16_f16 v[2:17], v[84:87], v[64:67], v[2:17]
	ds_read_b128 v[64:67], v45 offset:5152
	v_or_b32_e32 v47, 0x3c00, v46
	s_waitcnt vmcnt(7) lgkmcnt(4)
	v_mfma_f32_32x32x16_f16 v[18:33], v[56:59], v[72:75], v[18:33]
	ds_read_b128 v[56:59], v45 offset:32
	ds_write_b128 v44, v[80:83] offset:10240
	s_waitcnt vmcnt(6) lgkmcnt(5)
	v_mfma_f32_32x32x16_f16 v[18:33], v[96:99], v[112:115], v[18:33]
	ds_read_b128 v[80:83], v45 offset:7712
	v_mfma_f32_32x32x16_f16 v[18:33], v[96:99], v[72:75], v[18:33]
	ds_read_b128 v[84:87], v45 offset:2592
	ds_write_b128 v44, v[60:63] offset:15360
	s_waitcnt lgkmcnt(7)
	v_mfma_f32_32x32x16_f16 v[2:17], v[100:103], v[72:75], v[2:17]
	global_load_dwordx4 v[60:63], v47, s[4:5]
	global_load_dwordx4 v[92:95], v47, s[6:7]
	s_waitcnt lgkmcnt(6)
	v_mfma_f32_32x32x16_f16 v[2:17], v[104:107], v[112:115], v[2:17]
	v_mfma_f32_32x32x16_f16 v[2:17], v[104:107], v[72:75], v[2:17]
	s_waitcnt lgkmcnt(0)
	s_barrier
	ds_read_b128 v[72:75], v45 offset:15360
	v_or_b32_e32 v47, 0x4000, v46
	s_waitcnt vmcnt(7)
	v_mfma_f32_32x32x16_f16 v[18:33], v[64:67], v[76:79], v[18:33]
	global_load_dwordx4 v[64:67], v[36:37], off offset:576
	ds_read_b128 v[96:99], v45 offset:10240
	s_waitcnt vmcnt(7)
	v_mfma_f32_32x32x16_f16 v[18:33], v[56:59], v[88:91], v[18:33]
	ds_read_b128 v[100:103], v45 offset:17920
	v_mfma_f32_32x32x16_f16 v[18:33], v[56:59], v[76:79], v[18:33]
	global_load_dwordx4 v[56:59], v[34:35], off offset:576
	ds_read_b128 v[104:107], v45 offset:12800
	v_mfma_f32_32x32x16_f16 v[2:17], v[80:83], v[76:79], v[2:17]
	global_load_dwordx4 v[80:83], v47, s[4:5]
	global_load_dwordx4 v[112:115], v47, s[6:7]
	v_mfma_f32_32x32x16_f16 v[2:17], v[84:87], v[88:91], v[2:17]
	v_mfma_f32_32x32x16_f16 v[2:17], v[84:87], v[76:79], v[2:17]
	ds_read_b128 v[76:79], v45 offset:15392
	s_movk_i32 s66, 0x4400
	v_or_b32_e32 v47, 0x4400, v46
	s_waitcnt vmcnt(7) lgkmcnt(4)
	v_mfma_f32_32x32x16_f16 v[18:33], v[72:75], v[68:71], v[18:33]
	ds_read_b128 v[72:75], v45 offset:10272
	ds_write_b128 v44, v[48:51]
	s_waitcnt vmcnt(6) lgkmcnt(5)
	v_mfma_f32_32x32x16_f16 v[18:33], v[96:99], v[108:111], v[18:33]
	ds_read_b128 v[48:51], v45 offset:17952
	v_mfma_f32_32x32x16_f16 v[18:33], v[96:99], v[68:71], v[18:33]
	ds_read_b128 v[84:87], v45 offset:12832
	ds_write_b128 v44, v[52:55] offset:5120
	s_waitcnt lgkmcnt(7)
	v_mfma_f32_32x32x16_f16 v[2:17], v[100:103], v[68:71], v[2:17]
	global_load_dwordx4 v[52:55], v47, s[4:5]
	global_load_dwordx4 v[88:91], v47, s[6:7]
	s_waitcnt lgkmcnt(6)
	v_mfma_f32_32x32x16_f16 v[2:17], v[104:107], v[108:111], v[2:17]
	v_mfma_f32_32x32x16_f16 v[2:17], v[104:107], v[68:71], v[2:17]
	s_waitcnt lgkmcnt(0)
	s_barrier
	ds_read_b128 v[68:71], v45 offset:5120
	v_or_b32_e32 v47, 0x4800, v46
	s_waitcnt vmcnt(7)
	v_mfma_f32_32x32x16_f16 v[18:33], v[76:79], v[60:63], v[18:33]
	global_load_dwordx4 v[76:79], v[36:37], off offset:640
	ds_read_b128 v[96:99], v45
	s_waitcnt vmcnt(7)
	v_mfma_f32_32x32x16_f16 v[18:33], v[72:75], v[92:95], v[18:33]
	ds_read_b128 v[100:103], v45 offset:7680
	v_mfma_f32_32x32x16_f16 v[18:33], v[72:75], v[60:63], v[18:33]
	global_load_dwordx4 v[72:75], v[34:35], off offset:640
	ds_read_b128 v[104:107], v45 offset:2560
	v_mfma_f32_32x32x16_f16 v[2:17], v[48:51], v[60:63], v[2:17]
	global_load_dwordx4 v[48:51], v47, s[4:5]
	global_load_dwordx4 v[108:111], v47, s[6:7]
	v_mfma_f32_32x32x16_f16 v[2:17], v[84:87], v[92:95], v[2:17]
	v_mfma_f32_32x32x16_f16 v[2:17], v[84:87], v[60:63], v[2:17]
	ds_read_b128 v[60:63], v45 offset:5152
	v_or_b32_e32 v47, 0x4c00, v46
	s_waitcnt vmcnt(7) lgkmcnt(4)
	v_mfma_f32_32x32x16_f16 v[18:33], v[68:71], v[80:83], v[18:33]
	ds_read_b128 v[68:71], v45 offset:32
	ds_write_b128 v44, v[64:67] offset:10240
	s_waitcnt vmcnt(6) lgkmcnt(5)
	v_mfma_f32_32x32x16_f16 v[18:33], v[96:99], v[112:115], v[18:33]
	ds_read_b128 v[64:67], v45 offset:7712
	v_mfma_f32_32x32x16_f16 v[18:33], v[96:99], v[80:83], v[18:33]
	ds_read_b128 v[84:87], v45 offset:2592
	ds_write_b128 v44, v[56:59] offset:15360
	s_waitcnt lgkmcnt(7)
	v_mfma_f32_32x32x16_f16 v[2:17], v[100:103], v[80:83], v[2:17]
	global_load_dwordx4 v[56:59], v47, s[4:5]
	global_load_dwordx4 v[92:95], v47, s[6:7]
	s_waitcnt lgkmcnt(6)
	v_mfma_f32_32x32x16_f16 v[2:17], v[104:107], v[112:115], v[2:17]
	v_mfma_f32_32x32x16_f16 v[2:17], v[104:107], v[80:83], v[2:17]
	s_waitcnt lgkmcnt(0)
	s_barrier
	ds_read_b128 v[80:83], v45 offset:15360
	v_or_b32_e32 v47, 0x5000, v46
	s_waitcnt vmcnt(7)
	v_mfma_f32_32x32x16_f16 v[18:33], v[60:63], v[52:55], v[18:33]
	global_load_dwordx4 v[60:63], v[36:37], off offset:704
	ds_read_b128 v[96:99], v45 offset:10240
	s_waitcnt vmcnt(7)
	v_mfma_f32_32x32x16_f16 v[18:33], v[68:71], v[88:91], v[18:33]
	ds_read_b128 v[100:103], v45 offset:17920
	v_mfma_f32_32x32x16_f16 v[18:33], v[68:71], v[52:55], v[18:33]
	global_load_dwordx4 v[68:71], v[34:35], off offset:704
	ds_read_b128 v[104:107], v45 offset:12800
	v_mfma_f32_32x32x16_f16 v[2:17], v[64:67], v[52:55], v[2:17]
	global_load_dwordx4 v[64:67], v47, s[4:5]
	global_load_dwordx4 v[112:115], v47, s[6:7]
	v_mfma_f32_32x32x16_f16 v[2:17], v[84:87], v[88:91], v[2:17]
	v_mfma_f32_32x32x16_f16 v[2:17], v[84:87], v[52:55], v[2:17]
	ds_read_b128 v[52:55], v45 offset:15392
	v_or_b32_e32 v47, 0x5400, v46
	s_waitcnt vmcnt(7) lgkmcnt(4)
	v_mfma_f32_32x32x16_f16 v[18:33], v[80:83], v[48:51], v[18:33]
	ds_read_b128 v[80:83], v45 offset:10272
	ds_write_b128 v44, v[76:79]
	s_waitcnt vmcnt(6) lgkmcnt(5)
	v_mfma_f32_32x32x16_f16 v[18:33], v[96:99], v[108:111], v[18:33]
	ds_read_b128 v[76:79], v45 offset:17952
	v_mfma_f32_32x32x16_f16 v[18:33], v[96:99], v[48:51], v[18:33]
	ds_read_b128 v[84:87], v45 offset:12832
	ds_write_b128 v44, v[72:75] offset:5120
	s_waitcnt lgkmcnt(7)
	v_mfma_f32_32x32x16_f16 v[2:17], v[100:103], v[48:51], v[2:17]
	global_load_dwordx4 v[72:75], v47, s[4:5]
	global_load_dwordx4 v[88:91], v47, s[6:7]
	s_waitcnt lgkmcnt(6)
	v_mfma_f32_32x32x16_f16 v[2:17], v[104:107], v[108:111], v[2:17]
	v_mfma_f32_32x32x16_f16 v[2:17], v[104:107], v[48:51], v[2:17]
	s_waitcnt lgkmcnt(0)
	s_barrier
	ds_read_b128 v[48:51], v45 offset:5120
	v_or_b32_e32 v47, 0x5800, v46
	s_waitcnt vmcnt(7)
	v_mfma_f32_32x32x16_f16 v[18:33], v[52:55], v[56:59], v[18:33]
	global_load_dwordx4 v[52:55], v[36:37], off offset:768
	ds_read_b128 v[96:99], v45
	s_waitcnt vmcnt(7)
	v_mfma_f32_32x32x16_f16 v[18:33], v[80:83], v[92:95], v[18:33]
	ds_read_b128 v[100:103], v45 offset:7680
	v_mfma_f32_32x32x16_f16 v[18:33], v[80:83], v[56:59], v[18:33]
	global_load_dwordx4 v[80:83], v[34:35], off offset:768
	ds_read_b128 v[104:107], v45 offset:2560
	v_mfma_f32_32x32x16_f16 v[2:17], v[76:79], v[56:59], v[2:17]
	global_load_dwordx4 v[76:79], v47, s[4:5]
	global_load_dwordx4 v[108:111], v47, s[6:7]
	v_mfma_f32_32x32x16_f16 v[2:17], v[84:87], v[92:95], v[2:17]
	v_mfma_f32_32x32x16_f16 v[2:17], v[84:87], v[56:59], v[2:17]
	ds_read_b128 v[56:59], v45 offset:5152
	v_or_b32_e32 v47, 0x5c00, v46
	s_waitcnt vmcnt(7) lgkmcnt(4)
	v_mfma_f32_32x32x16_f16 v[18:33], v[48:51], v[64:67], v[18:33]
	ds_read_b128 v[48:51], v45 offset:32
	ds_write_b128 v44, v[60:63] offset:10240
	s_waitcnt vmcnt(6) lgkmcnt(5)
	v_mfma_f32_32x32x16_f16 v[18:33], v[96:99], v[112:115], v[18:33]
	ds_read_b128 v[60:63], v45 offset:7712
	v_mfma_f32_32x32x16_f16 v[18:33], v[96:99], v[64:67], v[18:33]
	ds_read_b128 v[84:87], v45 offset:2592
	ds_write_b128 v44, v[68:71] offset:15360
	s_waitcnt lgkmcnt(7)
	v_mfma_f32_32x32x16_f16 v[2:17], v[100:103], v[64:67], v[2:17]
	global_load_dwordx4 v[68:71], v47, s[4:5]
	global_load_dwordx4 v[92:95], v47, s[6:7]
	s_waitcnt lgkmcnt(6)
	v_mfma_f32_32x32x16_f16 v[2:17], v[104:107], v[112:115], v[2:17]
	v_mfma_f32_32x32x16_f16 v[2:17], v[104:107], v[64:67], v[2:17]
	s_waitcnt lgkmcnt(0)
	s_barrier
	ds_read_b128 v[64:67], v45 offset:15360
	v_or_b32_e32 v47, 0x6000, v46
	s_waitcnt vmcnt(7)
	v_mfma_f32_32x32x16_f16 v[18:33], v[56:59], v[72:75], v[18:33]
	global_load_dwordx4 v[56:59], v[36:37], off offset:832
	ds_read_b128 v[96:99], v45 offset:10240
	s_waitcnt vmcnt(7)
	v_mfma_f32_32x32x16_f16 v[18:33], v[48:51], v[88:91], v[18:33]
	ds_read_b128 v[100:103], v45 offset:17920
	v_mfma_f32_32x32x16_f16 v[18:33], v[48:51], v[72:75], v[18:33]
	global_load_dwordx4 v[48:51], v[34:35], off offset:832
	ds_read_b128 v[104:107], v45 offset:12800
	v_mfma_f32_32x32x16_f16 v[2:17], v[60:63], v[72:75], v[2:17]
	global_load_dwordx4 v[60:63], v47, s[4:5]
	global_load_dwordx4 v[112:115], v47, s[6:7]
	v_mfma_f32_32x32x16_f16 v[2:17], v[84:87], v[88:91], v[2:17]
	v_mfma_f32_32x32x16_f16 v[2:17], v[84:87], v[72:75], v[2:17]
	ds_read_b128 v[72:75], v45 offset:15392
	v_or_b32_e32 v47, 0x6400, v46
	s_waitcnt vmcnt(7) lgkmcnt(4)
	v_mfma_f32_32x32x16_f16 v[18:33], v[64:67], v[76:79], v[18:33]
	ds_read_b128 v[64:67], v45 offset:10272
	ds_write_b128 v44, v[52:55]
	s_waitcnt vmcnt(6) lgkmcnt(5)
	v_mfma_f32_32x32x16_f16 v[18:33], v[96:99], v[108:111], v[18:33]
	ds_read_b128 v[52:55], v45 offset:17952
	v_mfma_f32_32x32x16_f16 v[18:33], v[96:99], v[76:79], v[18:33]
	ds_read_b128 v[84:87], v45 offset:12832
	ds_write_b128 v44, v[80:83] offset:5120
	s_waitcnt lgkmcnt(7)
	v_mfma_f32_32x32x16_f16 v[2:17], v[100:103], v[76:79], v[2:17]
	global_load_dwordx4 v[80:83], v47, s[4:5]
	global_load_dwordx4 v[88:91], v47, s[6:7]
	s_waitcnt lgkmcnt(6)
	v_mfma_f32_32x32x16_f16 v[2:17], v[104:107], v[108:111], v[2:17]
	v_mfma_f32_32x32x16_f16 v[2:17], v[104:107], v[76:79], v[2:17]
	s_waitcnt lgkmcnt(0)
	s_barrier
	ds_read_b128 v[76:79], v45 offset:5120
	v_or_b32_e32 v47, 0x6800, v46
	s_waitcnt vmcnt(7)
	v_mfma_f32_32x32x16_f16 v[18:33], v[72:75], v[68:71], v[18:33]
	global_load_dwordx4 v[72:75], v[36:37], off offset:896
	ds_read_b128 v[96:99], v45
	s_waitcnt vmcnt(7)
	v_mfma_f32_32x32x16_f16 v[18:33], v[64:67], v[92:95], v[18:33]
	ds_read_b128 v[100:103], v45 offset:7680
	v_mfma_f32_32x32x16_f16 v[18:33], v[64:67], v[68:71], v[18:33]
	global_load_dwordx4 v[64:67], v[34:35], off offset:896
	ds_read_b128 v[104:107], v45 offset:2560
	v_mfma_f32_32x32x16_f16 v[2:17], v[52:55], v[68:71], v[2:17]
	global_load_dwordx4 v[52:55], v47, s[4:5]
	global_load_dwordx4 v[108:111], v47, s[6:7]
	v_mfma_f32_32x32x16_f16 v[2:17], v[84:87], v[92:95], v[2:17]
	v_mfma_f32_32x32x16_f16 v[2:17], v[84:87], v[68:71], v[2:17]
	ds_read_b128 v[68:71], v45 offset:5152
	v_or_b32_e32 v47, 0x6c00, v46
	s_waitcnt vmcnt(7) lgkmcnt(4)
	v_mfma_f32_32x32x16_f16 v[18:33], v[76:79], v[60:63], v[18:33]
	ds_read_b128 v[76:79], v45 offset:32
	ds_write_b128 v44, v[56:59] offset:10240
	s_waitcnt vmcnt(6) lgkmcnt(5)
	v_mfma_f32_32x32x16_f16 v[18:33], v[96:99], v[112:115], v[18:33]
	ds_read_b128 v[56:59], v45 offset:7712
	v_mfma_f32_32x32x16_f16 v[18:33], v[96:99], v[60:63], v[18:33]
	ds_read_b128 v[84:87], v45 offset:2592
	ds_write_b128 v44, v[48:51] offset:15360
	s_waitcnt lgkmcnt(7)
	v_mfma_f32_32x32x16_f16 v[2:17], v[100:103], v[60:63], v[2:17]
	global_load_dwordx4 v[48:51], v47, s[4:5]
	global_load_dwordx4 v[92:95], v47, s[6:7]
	s_waitcnt lgkmcnt(6)
	v_mfma_f32_32x32x16_f16 v[2:17], v[104:107], v[112:115], v[2:17]
	v_mfma_f32_32x32x16_f16 v[2:17], v[104:107], v[60:63], v[2:17]
	s_waitcnt lgkmcnt(0)
	s_barrier
	ds_read_b128 v[60:63], v45 offset:15360
	v_or_b32_e32 v47, 0x7000, v46
	s_waitcnt vmcnt(7)
	v_mfma_f32_32x32x16_f16 v[18:33], v[68:71], v[80:83], v[18:33]
	global_load_dwordx4 v[68:71], v[36:37], off offset:960
	ds_read_b128 v[96:99], v45 offset:10240
	s_waitcnt vmcnt(7)
	v_mfma_f32_32x32x16_f16 v[18:33], v[76:79], v[88:91], v[18:33]
	ds_read_b128 v[100:103], v45 offset:17920
	v_mfma_f32_32x32x16_f16 v[18:33], v[76:79], v[80:83], v[18:33]
	global_load_dwordx4 v[34:37], v[34:35], off offset:960
	ds_read_b128 v[76:79], v45 offset:12800
	v_mfma_f32_32x32x16_f16 v[2:17], v[56:59], v[80:83], v[2:17]
	global_load_dwordx4 v[56:59], v47, s[4:5]
	global_load_dwordx4 v[104:107], v47, s[6:7]
	v_mfma_f32_32x32x16_f16 v[2:17], v[84:87], v[88:91], v[2:17]
	v_mfma_f32_32x32x16_f16 v[2:17], v[84:87], v[80:83], v[2:17]
	ds_read_b128 v[80:83], v45 offset:15392
	v_or_b32_e32 v47, 0x7400, v46
	s_waitcnt vmcnt(7) lgkmcnt(4)
	v_mfma_f32_32x32x16_f16 v[18:33], v[60:63], v[52:55], v[18:33]
	ds_read_b128 v[60:63], v45 offset:10272
	ds_write_b128 v44, v[72:75]
	s_waitcnt vmcnt(6) lgkmcnt(5)
	v_mfma_f32_32x32x16_f16 v[18:33], v[96:99], v[108:111], v[18:33]
	ds_read_b128 v[72:75], v45 offset:17952
	v_mfma_f32_32x32x16_f16 v[18:33], v[96:99], v[52:55], v[18:33]
	ds_read_b128 v[84:87], v45 offset:12832
	ds_write_b128 v44, v[64:67] offset:5120
	s_waitcnt lgkmcnt(7)
	v_mfma_f32_32x32x16_f16 v[2:17], v[100:103], v[52:55], v[2:17]
	global_load_dwordx4 v[64:67], v47, s[4:5]
	global_load_dwordx4 v[88:91], v47, s[6:7]
	s_waitcnt lgkmcnt(6)
	v_mfma_f32_32x32x16_f16 v[2:17], v[76:79], v[108:111], v[2:17]
	v_mfma_f32_32x32x16_f16 v[2:17], v[76:79], v[52:55], v[2:17]
	s_waitcnt lgkmcnt(0)
	s_barrier
	ds_read_b128 v[52:55], v45 offset:5120
	v_or_b32_e32 v47, 0x7800, v46
	s_waitcnt vmcnt(7)
	v_mfma_f32_32x32x16_f16 v[18:33], v[80:83], v[48:51], v[18:33]
	ds_read_b128 v[76:79], v45
	s_waitcnt vmcnt(6)
	v_mfma_f32_32x32x16_f16 v[18:33], v[60:63], v[92:95], v[18:33]
	ds_read_b128 v[80:83], v45 offset:7680
	v_mfma_f32_32x32x16_f16 v[18:33], v[60:63], v[48:51], v[18:33]
	ds_read_b128 v[60:63], v45 offset:2560
	v_mfma_f32_32x32x16_f16 v[2:17], v[72:75], v[48:51], v[2:17]
	global_load_dwordx4 v[72:75], v47, s[4:5]
	global_load_dwordx4 v[96:99], v47, s[6:7]
	v_mfma_f32_32x32x16_f16 v[2:17], v[84:87], v[92:95], v[2:17]
	v_mfma_f32_32x32x16_f16 v[2:17], v[84:87], v[48:51], v[2:17]
	v_or_b32_e32 v100, 0x7c00, v46
	ds_read_b128 v[46:49], v45 offset:5152
	s_waitcnt vmcnt(5) lgkmcnt(4)
	v_mfma_f32_32x32x16_f16 v[18:33], v[52:55], v[56:59], v[18:33]
	ds_read_b128 v[50:53], v45 offset:32
	ds_write_b128 v44, v[68:71] offset:10240
	s_waitcnt vmcnt(4) lgkmcnt(5)
	v_mfma_f32_32x32x16_f16 v[18:33], v[76:79], v[104:107], v[18:33]
	ds_read_b128 v[84:87], v45 offset:7712
	v_mfma_f32_32x32x16_f16 v[18:33], v[76:79], v[56:59], v[18:33]
	ds_read_b128 v[76:79], v45 offset:2592
	ds_write_b128 v44, v[34:37] offset:15360
	s_waitcnt lgkmcnt(7)
	v_mfma_f32_32x32x16_f16 v[2:17], v[80:83], v[56:59], v[2:17]
	global_load_dwordx4 v[80:83], v100, s[4:5]
	global_load_dwordx4 v[92:95], v100, s[6:7]
	s_waitcnt lgkmcnt(6)
	v_mfma_f32_32x32x16_f16 v[2:17], v[60:63], v[104:107], v[2:17]
	v_mfma_f32_32x32x16_f16 v[2:17], v[60:63], v[56:59], v[2:17]
	s_waitcnt lgkmcnt(0)
	s_barrier
	ds_read_b128 v[54:57], v45 offset:15360
	s_waitcnt vmcnt(5)
	v_mfma_f32_32x32x16_f16 v[18:33], v[46:49], v[64:67], v[18:33]
	ds_read_b128 v[46:49], v45 offset:10240
	s_waitcnt vmcnt(4)
	v_mfma_f32_32x32x16_f16 v[18:33], v[50:53], v[88:91], v[18:33]
	ds_read_b128 v[58:61], v45 offset:17920
	v_mfma_f32_32x32x16_f16 v[18:33], v[50:53], v[64:67], v[18:33]
	ds_read_b128 v[50:53], v45 offset:12800
	v_mfma_f32_32x32x16_f16 v[2:17], v[84:87], v[64:67], v[2:17]
	v_mfma_f32_32x32x16_f16 v[2:17], v[76:79], v[88:91], v[2:17]
	v_mfma_f32_32x32x16_f16 v[2:17], v[76:79], v[64:67], v[2:17]
	ds_read_b128 v[62:65], v45 offset:15392
	s_waitcnt vmcnt(3) lgkmcnt(4)
	v_mfma_f32_32x32x16_f16 v[18:33], v[54:57], v[72:75], v[18:33]
	ds_read_b128 v[54:57], v45 offset:10272
	ds_write_b128 v44, v[68:71]
	s_waitcnt vmcnt(2) lgkmcnt(5)
	v_mfma_f32_32x32x16_f16 v[18:33], v[46:49], v[96:99], v[18:33]
	ds_read_b128 v[66:69], v45 offset:17952
	v_mfma_f32_32x32x16_f16 v[18:33], v[46:49], v[72:75], v[18:33]
	ds_read_b128 v[46:49], v45 offset:12832
	ds_write_b128 v44, v[34:37] offset:5120
	s_waitcnt lgkmcnt(7)
	v_mfma_f32_32x32x16_f16 v[2:17], v[58:61], v[72:75], v[2:17]
	s_waitcnt lgkmcnt(6)
	v_mfma_f32_32x32x16_f16 v[2:17], v[50:53], v[96:99], v[2:17]
	v_mfma_f32_32x32x16_f16 v[2:17], v[50:53], v[72:75], v[2:17]
	s_waitcnt lgkmcnt(0)
	s_barrier
	s_waitcnt vmcnt(1)
	v_mfma_f32_32x32x16_f16 v[18:33], v[62:65], v[80:83], v[18:33]
	s_waitcnt vmcnt(0)
	v_mfma_f32_32x32x16_f16 v[18:33], v[54:57], v[92:95], v[18:33]
	v_mfma_f32_32x32x16_f16 v[18:33], v[54:57], v[80:83], v[18:33]
	v_mfma_f32_32x32x16_f16 v[2:17], v[66:69], v[80:83], v[2:17]
	v_mfma_f32_32x32x16_f16 v[2:17], v[46:49], v[92:95], v[2:17]
	v_mfma_f32_32x32x16_f16 v[2:17], v[46:49], v[80:83], v[2:17]
	v_mul_u32_u24_e32 v34, 0x4400, v40
	v_lshlrev_b32_e32 v35, 7, v41
	v_lshlrev_b32_e32 v36, 2, v42
	v_or3_b32 v34, v34, v35, v36
	s_movk_i32 s2, 0x440
	s_nop 3
	v_fma_f32 v18, s19, v18, v39
	v_mad_u32_u24 v34, v43, s2, v34
	v_fma_f32 v19, s19, v19, v39
	s_barrier
	ds_write2_b32 v34, v18, v19 offset1:68
	v_fma_f32 v18, s19, v20, v39
	v_fma_f32 v19, s19, v21, v39
	ds_write2_b32 v34, v18, v19 offset0:136 offset1:204
	v_fma_f32 v18, s19, v22, v39
	v_fma_f32 v19, s19, v23, v39
	v_add_u32_e32 v20, 0x800, v34
	ds_write2_b32 v20, v18, v19 offset0:32 offset1:100
	v_fma_f32 v18, s19, v24, v39
	v_fma_f32 v19, s19, v25, v39
	ds_write2_b32 v20, v18, v19 offset0:168 offset1:236
	v_fma_f32 v18, s19, v26, v39
	v_fma_f32 v19, s19, v27, v39
	v_add_u32_e32 v20, 0x1000, v34
	ds_write2_b32 v20, v18, v19 offset0:64 offset1:132
	v_fma_f32 v18, s19, v28, v39
	v_fma_f32 v19, s19, v29, v39
	v_add_u32_e32 v20, 0x1200, v34
	ds_write2_b32 v20, v18, v19 offset0:72 offset1:140
	v_fma_f32 v18, s19, v30, v39
	v_fma_f32 v19, s19, v31, v39
	v_add_u32_e32 v20, 0x1800, v34
	ds_write2_b32 v20, v18, v19 offset0:96 offset1:164
	v_fma_f32 v18, s19, v32, v39
	v_fma_f32 v19, s19, v33, v39
	v_add_u32_e32 v20, 0x1a00, v34
	ds_write2_b32 v20, v18, v19 offset0:104 offset1:172
	v_fma_f32 v2, s19, v2, v39
	v_fma_f32 v3, s19, v3, v39
	v_add_u32_e32 v18, 0x2000, v34
	ds_write2_b32 v18, v2, v3 offset0:128 offset1:196
	v_fma_f32 v2, s19, v4, v39
	v_fma_f32 v3, s19, v5, v39
	v_add_u32_e32 v4, 0x2400, v34
	ds_write2_b32 v4, v2, v3 offset0:8 offset1:76
	v_fma_f32 v2, s19, v6, v39
	v_fma_f32 v3, s19, v7, v39
	v_add_u32_e32 v4, 0x2800, v34
	ds_write2_b32 v4, v2, v3 offset0:160 offset1:228
	v_fma_f32 v2, s19, v8, v39
	v_fma_f32 v3, s19, v9, v39
	v_add_u32_e32 v4, 0x2c00, v34
	ds_write2_b32 v4, v2, v3 offset0:40 offset1:108
	v_fma_f32 v2, s19, v10, v39
	v_fma_f32 v3, s19, v11, v39
	v_add_u32_e32 v4, 0x3200, v34
	ds_write2_b32 v4, v2, v3 offset0:64 offset1:132
	v_fma_f32 v2, s19, v12, v39
	v_fma_f32 v3, s19, v13, v39
	v_add_u32_e32 v4, 0x3400, v34
	s_sub_i32 s2, 0x100, s33
	ds_write2_b32 v4, v2, v3 offset0:72 offset1:140
	v_fma_f32 v2, s19, v14, v39
	v_fma_f32 v3, s19, v15, v39
	v_add_u32_e32 v4, 0x3a00, v34
	s_min_i32 s21, s21, s2
	ds_write2_b32 v4, v2, v3 offset0:96 offset1:164
	v_fma_f32 v2, s19, v16, v39
	v_fmac_f32_e32 v39, s19, v17
	v_add_u32_e32 v3, 0x3c00, v34
	v_cmp_gt_i32_e32 vcc, s21, v38
	ds_write2_b32 v3, v2, v39 offset0:104 offset1:172
	s_waitcnt lgkmcnt(0)
	s_barrier
	s_and_saveexec_b64 s[2:3], vcc
	s_cbranch_execz .LBB0_59
	v_lshlrev_b32_e32 v2, 2, v0
	v_and_b32_e32 v2, 12, v2
	v_or_b32_e32 v4, 1, v2
	v_lshrrev_b32_e32 v6, 2, v1
	v_cmp_gt_i32_e64 s[6:7], s20, v4
	v_or_b32_e32 v4, 2, v2
	s_load_dwordx4 s[24:27], s[0:1], 0x28
	v_cmp_gt_i32_e32 vcc, s20, v6
	v_cmp_le_i32_e64 s[0:1], s23, v6
	v_cmp_gt_i32_e64 s[10:11], s20, v4
	v_or_b32_e32 v4, 3, v2
	s_and_b64 s[0:1], vcc, s[0:1]
	v_cmp_gt_i32_e64 s[2:3], s20, v2
	v_cmp_gt_i32_e64 s[14:15], s20, v4
	s_and_b64 s[4:5], s[2:3], s[0:1]
	s_and_b64 s[8:9], s[0:1], s[6:7]
	s_and_b64 s[12:13], s[0:1], s[10:11]
	s_and_b64 s[16:17], s[0:1], s[14:15]
	s_cmp_gt_i32 s20, 0
	s_cselect_b64 s[28:29], -1, 0
	s_cmp_eq_u32 s18, 0
	s_cselect_b64 s[18:19], -1, 0
	s_cmp_lt_i32 s23, 1
	s_cselect_b64 s[30:31], -1, 0
	s_and_b64 s[30:31], s[30:31], s[28:29]
	s_cmp_lt_i32 s23, 2
	s_cselect_b64 s[34:35], -1, 0
	s_cmp_gt_i32 s20, 1
	s_cselect_b64 s[36:37], -1, 0
	s_and_b64 s[34:35], s[34:35], s[36:37]
	s_cmp_lt_i32 s23, 3
	s_cselect_b64 s[36:37], -1, 0
	s_cmp_gt_i32 s20, 2
	s_cselect_b64 s[38:39], -1, 0
	s_and_b64 s[36:37], s[36:37], s[38:39]
	s_cmp_lt_i32 s23, 4
	s_cselect_b64 s[38:39], -1, 0
	s_cmp_gt_i32 s20, 3
	s_cselect_b64 s[40:41], -1, 0
	s_and_b64 s[38:39], s[38:39], s[40:41]
	s_cmp_lt_i32 s23, 5
	s_cselect_b64 s[40:41], -1, 0
	s_cmp_gt_i32 s20, 4
	s_cselect_b64 s[42:43], -1, 0
	s_and_b64 s[40:41], s[40:41], s[42:43]
	s_cmp_lt_i32 s23, 6
	s_cselect_b64 s[42:43], -1, 0
	s_cmp_gt_i32 s20, 5
	s_cselect_b64 s[44:45], -1, 0
	s_and_b64 s[42:43], s[42:43], s[44:45]
	s_cmp_lt_i32 s23, 7
	s_cselect_b64 s[44:45], -1, 0
	s_cmp_gt_i32 s20, 6
	s_cselect_b64 s[46:47], -1, 0
	s_and_b64 s[44:45], s[44:45], s[46:47]
	s_cmp_lt_i32 s23, 8
	s_cselect_b64 s[46:47], -1, 0
	s_cmp_gt_i32 s20, 7
	s_cselect_b64 s[48:49], -1, 0
	s_and_b64 s[46:47], s[46:47], s[48:49]
	s_cmp_lt_i32 s23, 9
	s_cselect_b64 s[48:49], -1, 0
	s_cmp_gt_i32 s20, 8
	s_cselect_b64 s[50:51], -1, 0
	s_and_b64 s[48:49], s[48:49], s[50:51]
	s_cmp_lt_i32 s23, 10
	s_cselect_b64 s[50:51], -1, 0
	s_cmp_gt_i32 s20, 9
	s_cselect_b64 s[52:53], -1, 0
	s_and_b64 s[50:51], s[50:51], s[52:53]
	s_cmp_lt_i32 s23, 11
	s_cselect_b64 s[52:53], -1, 0
	s_cmp_gt_i32 s20, 10
	s_cselect_b64 s[54:55], -1, 0
	s_and_b64 s[52:53], s[52:53], s[54:55]
	s_cmp_lt_i32 s23, 12
	s_cselect_b64 s[54:55], -1, 0
	s_cmp_gt_i32 s20, 11
	s_cselect_b64 s[56:57], -1, 0
	s_and_b64 s[54:55], s[54:55], s[56:57]
	s_cmp_lt_i32 s23, 13
	s_cselect_b64 s[56:57], -1, 0
	s_cmp_gt_i32 s20, 12
	s_cselect_b64 s[58:59], -1, 0
	s_and_b64 s[56:57], s[56:57], s[58:59]
	s_cmp_lt_i32 s23, 14
	s_cselect_b64 s[58:59], -1, 0
	s_cmp_gt_i32 s20, 13
	s_cselect_b64 s[60:61], -1, 0
	s_and_b64 s[58:59], s[58:59], s[60:61]
	s_cmp_lt_i32 s23, 15
	s_cselect_b64 s[60:61], -1, 0
	s_cmp_gt_i32 s20, 14
	s_cselect_b64 s[62:63], -1, 0
	s_and_b64 s[60:61], s[60:61], s[62:63]
	s_cmp_lt_i32 s23, 16
	s_movk_i32 s67, 0x940
	v_mul_u32_u24_e32 v2, 0x50, v2
	v_or_b32_e32 v4, s22, v1
	s_cselect_b64 s[22:23], -1, 0
	s_cmp_gt_i32 s20, 15
	v_mad_u32_u24 v2, v38, s67, v2
	s_cselect_b64 s[62:63], -1, 0
	v_and_or_b32 v5, v1, 60, v2
	v_lshlrev_b32_e32 v2, 2, v1
	s_and_b64 s[22:23], s[22:23], s[62:63]
	v_mul_lo_u32 v1, s20, v38
	s_movk_i32 s73, 0x110
	v_and_b32_e32 v0, 3, v0
	s_cmp_lg_u32 s20, 1
	v_mul_lo_u32 v7, v1, s73
	v_mul_u32_u24_e32 v0, 0x440, v0
	s_cselect_b64 s[62:63], -1, 0
	s_and_b32 s72, s20, 0x7ffffffe
	v_add3_u32 v23, v7, v0, s66
	v_add_u32_e32 v0, v6, v1
	s_bitcmp1_b32 s20, 0
	v_mul_lo_u32 v24, v0, s73
	s_mov_b32 s66, 0x8800
	v_mov_b32_e32 v0, 0xd040
	v_mul_u32_u24_e32 v3, 0x940, v38
	v_add_u32_e32 v20, 0x50, v5
	v_add_u32_e32 v21, 0xa0, v5
	v_add_u32_e32 v22, 0xf0, v5
	s_cselect_b64 s[64:65], -1, 0
	s_mul_i32 s74, s20, 0x660
	v_add3_u32 v25, v7, v2, s66
	v_mad_u32_u24 v26, v38, s67, v0
	s_mov_b64 s[66:67], 0
	s_mov_b32 s68, 0x3e000000
	s_mov_b32 s75, 0x3fb8aa3b
	s_mov_b32 s76, 0xc2ce8ed0
	s_mov_b32 s77, 0x42b17218
	s_mov_b32 s78, 0x43800000
	v_mov_b32_e32 v27, 0xff800000
	v_mov_b32_e32 v28, 0x7f800000
	s_branch .LBB0_7

.LBB0_59:
	s_endpgm
	s_endpgm
	s_endpgm
	s_endpgm
	s_endpgm
	s_endpgm
	s_endpgm
	s_endpgm
	s_endpgm
	s_endpgm
	s_endpgm
	s_endpgm
	s_endpgm
	s_endpgm
	s_endpgm
	s_endpgm
	s_endpgm
	s_endpgm
	s_endpgm
	s_endpgm
	s_endpgm
	s_endpgm
	s_endpgm
	s_endpgm
	s_endpgm
	s_endpgm
	.section	.rodata,"a",@progbits
	.p2align	6, 0x0
